# all small edits together on v91: MoE gate/up counted waits, router bias preload, cross-attention reads one MFMA ahead, FIN wave sums by DPP, leader early invalidate, per-XCD release counter replicas
# speedup vs baseline: 1.0107x; 1.0058x over previous
; __device__ __forceinline__ unsigned xb_ld(unsigned* p)              { return __hip_atomic_load(p, __ATOMIC_RELAXED, __HIP_MEMORY_SCOPE_AGENT); }
; __device__ __forceinline__ unsigned xb_add(unsigned* p, unsigned v) { return __hip_atomic_fetch_add(p, v, __ATOMIC_RELAXED, __HIP_MEMORY_SCOPE_AGENT); }
; #define XB_SPIN(cond, bar) do { unsigned _sp = 0; while (cond) { __builtin_amdgcn_s_sleep(1); \
;     if ((++_sp & 255u) == 0u) { if (xb_ld(&(bar)[XB_TMO])) break; if (_sp > XB_SPIN_CAP) { atomicAdd(&(bar)[XB_TMO], 1u); break; } } } } while (0)
; __device__ __forceinline__ void xcd_barrier(const XcdBarrier& b, const int wv) {
;     ...
;         const unsigned old = xb_add(&bar[XB_XSUB(bx)], 1u);
;         const unsigned gen = old / nloc;
;         if (old + 1u == (gen + 1u) * nloc) {
;             __builtin_amdgcn_fence(__ATOMIC_RELEASE, "agent");
;             asm volatile("s_waitcnt vmcnt(0)" ::: "memory");
;             const unsigned og = xb_add(&bar[XB_TOP], 1u);
;             const unsigned tg = og / nx;
;             __builtin_amdgcn_fence(__ATOMIC_ACQUIRE, "agent");
;             if (og + 1u == (tg + 1u) * nx) xb_add(&bar[XB_TOPGEN], 1u);
;             else XB_SPIN(xb_ld(&bar[XB_TOPGEN]) == tg, bar);
;             asm volatile("s_waitcnt vmcnt(0)" ::: "memory");
;         } else {
;             __builtin_amdgcn_fence(__ATOMIC_ACQUIRE, "agent");
;             XB_SPIN(xb_ld(&bar[XB_TOPGEN]) == gen, bar);
;             asm volatile("s_waitcnt vmcnt(0)" ::: "memory");
;         }
.LBB0_185:
	s_andn2_saveexec_b64 s[6:7], s[6:7]
	s_cbranch_execz .LBB0_205
	s_mov_b64 s[6:7], exec
	buffer_wbl2 sc1
	s_waitcnt vmcnt(0) lgkmcnt(0)
	s_waitcnt vmcnt(0)
	buffer_inv sc1
	v_mbcnt_lo_u32_b32 v2, s6, 0
	v_mbcnt_hi_u32_b32 v2, s7, v2
	v_cmp_eq_u32_e32 vcc, 0, v2
	s_and_saveexec_b64 s[8:9], vcc
	s_cbranch_execz .LBB0_188
	s_add_u32 s12, s4, 0x2400
	s_addc_u32 s13, s5, 0
	v_mov_b32_e32 v5, 0
	v_mov_b32_e32 v6, 1
	global_atomic_add v5, v6, s[12:13]
	global_atomic_add v5, v6, s[12:13] offset:256
	global_atomic_add v5, v6, s[12:13] offset:512
	global_atomic_add v5, v6, s[12:13] offset:768
	global_atomic_add v5, v6, s[12:13] offset:1024
	global_atomic_add v5, v6, s[12:13] offset:1280
	global_atomic_add v5, v6, s[12:13] offset:1536
	global_atomic_add v5, v6, s[12:13] offset:1792
	global_atomic_add v5, v6, s[12:13] offset:2048
	global_atomic_add v5, v6, s[12:13] offset:2304
	global_atomic_add v5, v6, s[12:13] offset:2560
	global_atomic_add v5, v6, s[12:13] offset:2816
	global_atomic_add v5, v6, s[12:13] offset:3072
	global_atomic_add v5, v6, s[12:13] offset:3328
	global_atomic_add v5, v6, s[12:13] offset:3584
	global_atomic_add v5, v6, s[12:13] offset:3840
	s_bcnt1_i32_b64 s6, s[6:7]
	v_mov_b32_e32 v3, 0x3000
	v_mov_b32_e32 v4, s6
	global_atomic_add v3, v3, v4, s[4:5] offset:1024 sc0
.LBB0_188:
	s_or_b64 exec, exec, s[8:9]
	v_cvt_f32_u32_e32 v4, v1
	s_waitcnt vmcnt(0)
	v_readfirstlane_b32 s6, v3
	s_lshl_b32 s8, s20, 8
	s_addk_i32 s8, 0x2400
	s_add_u32 s8, s4, s8
	s_addc_u32 s9, s5, 0
	v_rcp_iflag_f32_e32 v4, v4
	v_add_u32_e32 v2, s6, v2
	s_mov_b64 s[10:11], 0
	v_mul_f32_e32 v3, 0x4f7ffffe, v4
	v_cvt_u32_f32_e32 v3, v3
	v_sub_u32_e32 v4, 0, v1
	v_mul_lo_u32 v4, v4, v3
	v_mul_hi_u32 v4, v3, v4
	v_add_u32_e32 v3, v3, v4
	v_mul_hi_u32 v3, v2, v3
	v_mul_lo_u32 v4, v3, v1
	v_sub_u32_e32 v4, v2, v4
	v_add_u32_e32 v5, 1, v3
	v_cmp_ge_u32_e32 vcc, v4, v1
	v_add_u32_e32 v2, 1, v2
	s_nop 0
	v_cndmask_b32_e32 v3, v3, v5, vcc
	v_sub_u32_e32 v5, v4, v1
	v_cndmask_b32_e32 v4, v4, v5, vcc
	v_add_u32_e32 v5, 1, v3
	v_cmp_ge_u32_e32 vcc, v4, v1
	s_nop 1
	v_cndmask_b32_e32 v4, v3, v5, vcc
	v_mul_lo_u32 v3, v1, v4
	v_add_u32_e32 v1, v3, v1
	v_cmp_ne_u32_e32 vcc, v2, v1
	v_mov_b32_e32 v5, v1
	v_mov_b64_e32 v[2:3], s[8:9]
	s_and_saveexec_b64 s[6:7], vcc
	s_cbranch_execz .LBB0_202
	v_mov_b32_e32 v1, 0
	global_load_dword v2, v1, s[8:9] sc1
	s_mov_b64 s[14:15], 0
	s_waitcnt vmcnt(0)
	v_cmp_lt_u32_e32 vcc, v2, v5
	s_and_saveexec_b64 s[12:13], vcc
	s_cbranch_execz .LBB0_201
	s_add_u32 s10, s4, 0x200
	s_addc_u32 s11, s5, 0
	s_mov_b32 s22, 1
	s_mov_b64 s[4:5], 0
	s_branch .LBB0_192

; __device__ __forceinline__ unsigned xb_ld(unsigned* p)              { return __hip_atomic_load(p, __ATOMIC_RELAXED, __HIP_MEMORY_SCOPE_AGENT); }
; __device__ __forceinline__ unsigned xb_add(unsigned* p, unsigned v) { return __hip_atomic_fetch_add(p, v, __ATOMIC_RELAXED, __HIP_MEMORY_SCOPE_AGENT); }
; #define XB_SPIN(cond, bar) do { unsigned _sp = 0; while (cond) { __builtin_amdgcn_s_sleep(1); \
;     if ((++_sp & 255u) == 0u) { if (xb_ld(&(bar)[XB_TMO])) break; if (_sp > XB_SPIN_CAP) { atomicAdd(&(bar)[XB_TMO], 1u); break; } } } } while (0)
; __device__ __forceinline__ void xcd_barrier(const XcdBarrier& b, const int wv) {
;     ...
;         const unsigned old = xb_add(&bar[XB_XSUB(bx)], 1u);
;         const unsigned gen = old / nloc;
;         if (old + 1u == (gen + 1u) * nloc) {
;             __builtin_amdgcn_fence(__ATOMIC_RELEASE, "agent");
;             asm volatile("s_waitcnt vmcnt(0)" ::: "memory");
;             const unsigned og = xb_add(&bar[XB_TOP], 1u);
;             const unsigned tg = og / nx;
;             __builtin_amdgcn_fence(__ATOMIC_ACQUIRE, "agent");
;             if (og + 1u == (tg + 1u) * nx) xb_add(&bar[XB_TOPGEN], 1u);
;             else XB_SPIN(xb_ld(&bar[XB_TOPGEN]) == tg, bar);
;             asm volatile("s_waitcnt vmcnt(0)" ::: "memory");
;         } else {
;             __builtin_amdgcn_fence(__ATOMIC_ACQUIRE, "agent");
;             XB_SPIN(xb_ld(&bar[XB_TOPGEN]) == gen, bar);
;             asm volatile("s_waitcnt vmcnt(0)" ::: "memory");
;         }
.LBB0_384:
	s_andn2_saveexec_b64 s[4:5], s[4:5]
	s_cbranch_execz .LBB0_402
	s_mov_b64 s[4:5], exec
	buffer_wbl2 sc1
	s_waitcnt vmcnt(0) lgkmcnt(0)
	s_waitcnt vmcnt(0)
	buffer_inv sc1
	v_mbcnt_lo_u32_b32 v1, s4, 0
	v_mbcnt_hi_u32_b32 v1, s5, v1
	v_cmp_eq_u32_e32 vcc, 0, v1
	s_and_saveexec_b64 s[6:7], vcc
	s_cbranch_execz .LBB0_387
	s_add_u32 s10, s2, 0x2400
	s_addc_u32 s11, s3, 0
	global_atomic_add v65, v227, s[10:11]
	global_atomic_add v65, v227, s[10:11] offset:256
	global_atomic_add v65, v227, s[10:11] offset:512
	global_atomic_add v65, v227, s[10:11] offset:768
	global_atomic_add v65, v227, s[10:11] offset:1024
	global_atomic_add v65, v227, s[10:11] offset:1280
	global_atomic_add v65, v227, s[10:11] offset:1536
	global_atomic_add v65, v227, s[10:11] offset:1792
	global_atomic_add v65, v227, s[10:11] offset:2048
	global_atomic_add v65, v227, s[10:11] offset:2304
	global_atomic_add v65, v227, s[10:11] offset:2560
	global_atomic_add v65, v227, s[10:11] offset:2816
	global_atomic_add v65, v227, s[10:11] offset:3072
	global_atomic_add v65, v227, s[10:11] offset:3328
	global_atomic_add v65, v227, s[10:11] offset:3584
	global_atomic_add v65, v227, s[10:11] offset:3840
	s_bcnt1_i32_b64 s4, s[4:5]
	v_mov_b32_e32 v2, s4
	v_mov_b32_e32 v3, 0x3000
	global_atomic_add v2, v3, v2, s[2:3] offset:1024 sc0
.LBB0_387:
	s_or_b64 exec, exec, s[6:7]
	v_cvt_f32_u32_e32 v3, v0
	s_waitcnt vmcnt(0)
	v_readfirstlane_b32 s4, v2
	s_lshl_b32 s6, s18, 8
	s_addk_i32 s6, 0x2400
	s_add_u32 s6, s2, s6
	s_addc_u32 s7, s3, 0
	v_rcp_iflag_f32_e32 v3, v3
	v_add_u32_e32 v1, s4, v1
	s_mov_b64 s[8:9], 0
	v_mul_f32_e32 v2, 0x4f7ffffe, v3
	v_cvt_u32_f32_e32 v2, v2
	v_sub_u32_e32 v3, 0, v0
	v_mul_lo_u32 v3, v3, v2
	v_mul_hi_u32 v3, v2, v3
	v_add_u32_e32 v2, v2, v3
	v_mul_hi_u32 v2, v1, v2
	v_mul_lo_u32 v3, v2, v0
	v_sub_u32_e32 v3, v1, v3
	v_add_u32_e32 v4, 1, v2
	v_cmp_ge_u32_e32 vcc, v3, v0
	v_add_u32_e32 v1, 1, v1
	s_nop 0
	v_cndmask_b32_e32 v2, v2, v4, vcc
	v_sub_u32_e32 v4, v3, v0
	v_cndmask_b32_e32 v3, v3, v4, vcc
	v_add_u32_e32 v4, 1, v2
	v_cmp_ge_u32_e32 vcc, v3, v0
	s_nop 1
	v_cndmask_b32_e32 v2, v2, v4, vcc
	v_mul_lo_u32 v3, v0, v2
	v_add_u32_e32 v0, v3, v0
	v_cmp_ne_u32_e32 vcc, v1, v0
	v_mov_b32_e32 v3, v0
	v_mov_b64_e32 v[0:1], s[6:7]
	s_and_saveexec_b64 s[4:5], vcc
	s_cbranch_execz .LBB0_399
	global_load_dword v0, v65, s[6:7] sc1
	s_mov_b64 s[12:13], 0
	s_waitcnt vmcnt(0)
	v_cmp_lt_u32_e32 vcc, v0, v3
	s_and_saveexec_b64 s[10:11], vcc
	s_cbranch_execz .LBB0_398
	s_add_u32 s8, s2, 0x200
	s_addc_u32 s9, s3, 0
	s_mov_b32 s20, 1
	s_mov_b64 s[2:3], 0
	s_branch .LBB0_391
